# speedup vs baseline: 1.0013x; 1.0013x over previous
.LBB3_14:
	s_add_i32 s0, s90, 0x2000
	s_cmpk_lg_i32 s90, 0x4000
	s_cselect_b32 s80, s0, 0
	s_add_i32 s0, s91, 2
	s_add_u32 s78, s76, 0x4000
	s_addc_u32 s79, s77, 0
	s_add_i32 s1, s91, 4
	s_add_u32 s76, s76, 0x8000
	s_addc_u32 s77, s77, 0
	s_cmp_lt_i32 s1, s89
	s_cselect_b32 s76, s78, s76
	s_cselect_b32 s77, s79, s77
	s_cselect_b32 s91, s0, s91
	s_cselect_b32 s0, s92, s0
	s_cselect_b32 s96, s90, s96
	s_cselect_b32 s92, s80, s92
	s_cbranch_scc1 .LBB3_4
	s_branch .LBB3_24
